# attention loop: removed 122 false-hazard s_nop 0, split 64 v_pk_add_f32 into v_add_f32 pairs
# speedup vs baseline: 1.0015x; 1.0015x over previous
.LBB0_734:
	s_waitcnt lgkmcnt(0)
	s_barrier
	ds_read_b128 v[64:67], v201 offset:0
	ds_read_b128 v[68:71], v202 offset:0
	ds_read_b128 v[72:75], v203 offset:0
	ds_read_b128 v[76:79], v204 offset:0
	ds_read_b128 v[162:165], v205 offset:0
	ds_read_b128 v[166:169], v206 offset:0
	s_waitcnt lgkmcnt(4)
	v_mfma_f32_32x32x16_bf16 v[80:95], v[64:67], v[96:99], 0
	ds_read_b128 v[170:173], v207 offset:0
	s_add_u32 s16, s22, s10
	v_mfma_f32_32x32x16_bf16 v[80:95], v[68:71], v[100:103], v[80:95]
	ds_read_b128 v[64:67], v208 offset:0
	s_waitcnt vmcnt(4)
	ds_write_b128 v225, v[136:139] offset:0x8000
	s_addc_u32 s17, s23, s11
	s_waitcnt lgkmcnt(5)
	v_mfma_f32_32x32x16_bf16 v[80:95], v[72:75], v[104:107], v[80:95]
	ds_read_b128 v[136:139], v201 offset:0x2000
	ds_write_b128 v226, v[140:143] offset:0x8000
	s_add_u32 s15, s22, s12
	v_mfma_f32_32x32x16_bf16 v[80:95], v[76:79], v[108:111], v[80:95]
	ds_read_b128 v[174:177], v202 offset:0x2000
	ds_write_b64 v227, v[132:133] offset:0x8000
	s_addc_u32 s14, s23, s13
	s_waitcnt lgkmcnt(7)
	v_mfma_f32_32x32x16_bf16 v[80:95], v[162:165], v[112:115], v[80:95]
	ds_read_b128 v[178:181], v203 offset:0x2000
	ds_write_b64 v228, v[134:135] offset:0x8000
	s_add_u32 s6, s15, 0x23a40000
	v_mfma_f32_32x32x16_bf16 v[80:95], v[166:169], v[116:119], v[80:95]
	ds_read_b128 v[162:165], v204 offset:0x2000
	ds_write_b64 v229, v[128:129] offset:0x8000
	s_addc_u32 s7, s14, 0
	s_waitcnt lgkmcnt(9)
	v_mfma_f32_32x32x16_bf16 v[80:95], v[170:173], v[120:123], v[80:95]
	ds_read_b128 v[166:169], v205 offset:0x2000
	ds_write_b64 v184, v[130:131] offset:0x8000
	s_add_u32 s8, s16, 0x3bc00200
	v_mfma_f32_32x32x16_bf16 v[80:95], v[64:67], v[124:127], v[80:95]
	ds_read_b128 v[170:173], v206 offset:0x2000
	s_waitcnt lgkmcnt(8)
	v_mfma_f32_32x32x16_bf16 v[64:79], v[136:139], v[96:99], 0
	ds_read_b128 v[230:233], v207 offset:0x2000
	s_addc_u32 s9, s17, 0
	global_load_dwordx4 v[132:135], v198, s[8:9]
	global_load_dwordx4 v[128:131], v199, s[8:9]
	global_load_dwordx4 v[140:143], v196, s[6:7]
	global_load_dwordx4 v[136:139], v197, s[6:7]
	v_mfma_f32_32x32x16_bf16 v[64:79], v[174:177], v[100:103], v[64:79]
	ds_read_b128 v[234:237], v208 offset:0x2000
	s_add_u32 s6, s16, 0x3bc00280
	v_exp_f32_e32 v80, v80
	v_exp_f32_e32 v81, v81
	v_exp_f32_e32 v82, v82
	v_exp_f32_e32 v83, v83
	s_waitcnt lgkmcnt(6)
	v_mfma_f32_32x32x16_bf16 v[64:79], v[178:181], v[104:107], v[64:79]
	s_addc_u32 s7, s17, 0
	v_exp_f32_e32 v84, v84
	v_exp_f32_e32 v85, v85
	v_exp_f32_e32 v86, v86
	v_exp_f32_e32 v87, v87
	v_mfma_f32_32x32x16_bf16 v[64:79], v[162:165], v[108:111], v[64:79]
	s_add_u32 s8, s15, 0x23a50000
	v_add_f32_e32 v160, v160, v80
	v_add_f32_e32 v161, v161, v81
	s_addc_u32 s9, s14, 0
	v_add_f32_e32 v160, v82, v160
	v_add_f32_e32 v161, v83, v161
	v_add_f32_e32 v160, v84, v160
	v_add_f32_e32 v161, v85, v161
	v_add_f32_e32 v182, v86, v160
	v_add_f32_e32 v183, v87, v161
	v_cvt_pk_bf16_f32 v160, v80, v81
	v_cvt_pk_bf16_f32 v161, v82, v83
	v_cvt_pk_bf16_f32 v162, v84, v85
	v_cvt_pk_bf16_f32 v163, v86, v87
	s_waitcnt lgkmcnt(2)
	v_mfma_f32_32x32x16_bf16 v[64:79], v[166:169], v[112:115], v[64:79]
	ds_read_b128 v[164:167], v209 offset:0
	ds_read_b128 v[174:177], v210 offset:0
	v_mfma_f32_32x32x16_bf16 v[64:79], v[170:173], v[116:119], v[64:79]
	v_exp_f32_e32 v88, v88
	v_exp_f32_e32 v89, v89
	v_exp_f32_e32 v90, v90
	v_exp_f32_e32 v91, v91
	ds_read_b128 v[168:171], v209 offset:0x1000
	ds_read_b128 v[178:181], v210 offset:0x1000
	s_waitcnt lgkmcnt(4)
	v_mfma_f32_32x32x16_bf16 v[64:79], v[230:233], v[120:123], v[64:79]
	v_exp_f32_e32 v92, v92
	v_exp_f32_e32 v93, v93
	v_exp_f32_e32 v94, v94
	v_exp_f32_e32 v95, v95
	v_add_f32_e32 v172, v182, v88
	v_add_f32_e32 v173, v183, v89
	v_cvt_pk_bf16_f32 v230, v88, v89
	v_cvt_pk_bf16_f32 v231, v90, v91
	v_cvt_pk_bf16_f32 v232, v92, v93
	v_cvt_pk_bf16_f32 v233, v94, v95
	v_mfma_f32_32x32x16_bf16 v[64:79], v[234:237], v[124:127], v[64:79]
	v_add_f32_e32 v172, v90, v172
	v_add_f32_e32 v173, v91, v173
	v_add_f32_e32 v172, v92, v172
	v_add_f32_e32 v173, v93, v173
	v_add_f32_e32 v172, v94, v172
	v_add_f32_e32 v173, v95, v173
	s_waitcnt lgkmcnt(2)
	v_mfma_f32_32x32x16_bf16 v[48:63], v[164:167], v[160:163], v[48:63]
	v_mfma_f32_32x32x16_bf16 v[48:63], v[174:177], v[230:233], v[48:63]
	ds_read_b128 v[80:83], v209 offset:0x2000
	ds_read_b128 v[84:87], v210 offset:0x2000
	s_waitcnt lgkmcnt(2)
	v_mfma_f32_32x32x16_bf16 v[32:47], v[168:171], v[160:163], v[32:47]
	v_mfma_f32_32x32x16_bf16 v[32:47], v[178:181], v[230:233], v[32:47]
	ds_read_b128 v[88:91], v209 offset:0x3000
	ds_read_b128 v[92:95], v210 offset:0x3000
	v_exp_f32_e32 v64, v64
	v_exp_f32_e32 v65, v65
	v_exp_f32_e32 v66, v66
	v_exp_f32_e32 v67, v67
	v_exp_f32_e32 v68, v68
	v_exp_f32_e32 v69, v69
	v_exp_f32_e32 v70, v70
	v_exp_f32_e32 v71, v71
	v_add_f32_e32 v164, v172, v64
	v_add_f32_e32 v165, v173, v65
	v_add_f32_e32 v164, v66, v164
	v_add_f32_e32 v165, v67, v165
	v_add_f32_e32 v164, v68, v164
	v_add_f32_e32 v165, v69, v165
	v_add_f32_e32 v168, v70, v164
	v_add_f32_e32 v169, v71, v165
	v_cvt_pk_bf16_f32 v164, v64, v65
	v_cvt_pk_bf16_f32 v165, v66, v67
	v_cvt_pk_bf16_f32 v166, v68, v69
	v_cvt_pk_bf16_f32 v167, v70, v71
	s_waitcnt lgkmcnt(2)
	v_mfma_f32_32x32x16_bf16 v[16:31], v[80:83], v[160:163], v[16:31]
	v_mfma_f32_32x32x16_bf16 v[16:31], v[84:87], v[230:233], v[16:31]
	ds_read_b128 v[80:83], v211 offset:0
	ds_read_b128 v[84:87], v224 offset:0
	s_waitcnt lgkmcnt(2)
	v_mfma_f32_32x32x16_bf16 v[0:15], v[88:91], v[160:163], v[0:15]
	v_mfma_f32_32x32x16_bf16 v[0:15], v[92:95], v[230:233], v[0:15]
	ds_read_b128 v[88:91], v211 offset:0x1000
	ds_read_b128 v[92:95], v224 offset:0x1000
	v_exp_f32_e32 v72, v72
	v_exp_f32_e32 v73, v73
	v_exp_f32_e32 v74, v74
	v_exp_f32_e32 v75, v75
	v_exp_f32_e32 v76, v76
	v_exp_f32_e32 v77, v77
	v_exp_f32_e32 v78, v78
	v_exp_f32_e32 v79, v79
	v_add_f32_e32 v160, v168, v72
	v_add_f32_e32 v161, v169, v73
	v_add_f32_e32 v160, v74, v160
	v_add_f32_e32 v161, v75, v161
	v_add_f32_e32 v160, v76, v160
	v_add_f32_e32 v161, v77, v161
	v_add_f32_e32 v194, v78, v160
	v_add_f32_e32 v195, v79, v161
	v_cvt_pk_bf16_f32 v160, v72, v73
	v_cvt_pk_bf16_f32 v161, v74, v75
	v_cvt_pk_bf16_f32 v162, v76, v77
	v_cvt_pk_bf16_f32 v163, v78, v79
	s_waitcnt lgkmcnt(2)
	v_mfma_f32_32x32x16_bf16 v[48:63], v[80:83], v[164:167], v[48:63]
	v_mfma_f32_32x32x16_bf16 v[48:63], v[84:87], v[160:163], v[48:63]
	ds_read_b128 v[64:67], v211 offset:0x2000
	ds_read_b128 v[68:71], v224 offset:0x2000
	s_waitcnt lgkmcnt(2)
	v_mfma_f32_32x32x16_bf16 v[32:47], v[88:91], v[164:167], v[32:47]
	v_mfma_f32_32x32x16_bf16 v[32:47], v[92:95], v[160:163], v[32:47]
	ds_read_b128 v[72:75], v211 offset:0x3000
	ds_read_b128 v[76:79], v224 offset:0x3000
	s_waitcnt lgkmcnt(2)
	v_mfma_f32_32x32x16_bf16 v[16:31], v[64:67], v[164:167], v[16:31]
	v_mfma_f32_32x32x16_bf16 v[16:31], v[68:71], v[160:163], v[16:31]
	s_waitcnt lgkmcnt(0)
	v_mfma_f32_32x32x16_bf16 v[0:15], v[72:75], v[164:167], v[0:15]
	v_mfma_f32_32x32x16_bf16 v[0:15], v[76:79], v[160:163], v[0:15]
	ds_read_b128 v[64:67], v201 offset:0x4000
	ds_read_b128 v[68:71], v202 offset:0x4000
	ds_read_b128 v[72:75], v203 offset:0x4000
	ds_read_b128 v[76:79], v204 offset:0x4000
	ds_read_b128 v[160:163], v205 offset:0x4000
	ds_read_b128 v[164:167], v206 offset:0x4000
	s_waitcnt lgkmcnt(4)
	v_mfma_f32_32x32x16_bf16 v[80:95], v[64:67], v[96:99], 0
	ds_read_b128 v[230:233], v207 offset:0x4000
	v_mfma_f32_32x32x16_bf16 v[80:95], v[68:71], v[100:103], v[80:95]
	ds_read_b128 v[64:67], v208 offset:0x4000
	s_waitcnt vmcnt(4)
	ds_write_b128 v225, v[152:155] offset:0xc000
	s_waitcnt lgkmcnt(5)
	v_mfma_f32_32x32x16_bf16 v[80:95], v[72:75], v[104:107], v[80:95]
	ds_read_b128 v[152:155], v201 offset:0x6000
	ds_write_b128 v226, v[156:159] offset:0xc000
	v_mfma_f32_32x32x16_bf16 v[80:95], v[76:79], v[108:111], v[80:95]
	ds_read_b128 v[180:183], v202 offset:0x6000
	ds_write_b64 v227, v[148:149] offset:0xc000
	s_waitcnt lgkmcnt(7)
	v_mfma_f32_32x32x16_bf16 v[80:95], v[160:163], v[112:115], v[80:95]
	ds_read_b128 v[176:179], v203 offset:0x6000
	ds_write_b64 v228, v[150:151] offset:0xc000
	v_mfma_f32_32x32x16_bf16 v[80:95], v[164:167], v[116:119], v[80:95]
	ds_read_b128 v[172:175], v204 offset:0x6000
	ds_write_b64 v229, v[144:145] offset:0xc000
	s_waitcnt lgkmcnt(9)
	v_mfma_f32_32x32x16_bf16 v[80:95], v[230:233], v[120:123], v[80:95]
	ds_read_b128 v[168:171], v205 offset:0x6000
	ds_write_b64 v184, v[146:147] offset:0xc000
	v_mfma_f32_32x32x16_bf16 v[80:95], v[64:67], v[124:127], v[80:95]
	ds_read_b128 v[164:167], v206 offset:0x6000
	s_waitcnt lgkmcnt(8)
	v_mfma_f32_32x32x16_bf16 v[64:79], v[152:155], v[96:99], 0
	ds_read_b128 v[160:163], v207 offset:0x6000
	global_load_dwordx4 v[148:151], v198, s[6:7]
	global_load_dwordx4 v[144:147], v199, s[6:7]
	global_load_dwordx4 v[156:159], v196, s[8:9]
	global_load_dwordx4 v[152:155], v197, s[8:9]
	s_add_u32 s6, s16, 0x3bc00300
	v_mfma_f32_32x32x16_bf16 v[64:79], v[180:183], v[100:103], v[64:79]
	ds_read_b128 v[230:233], v208 offset:0x6000
	s_addc_u32 s7, s17, 0
	v_exp_f32_e32 v80, v80
	v_exp_f32_e32 v81, v81
	v_exp_f32_e32 v82, v82
	v_exp_f32_e32 v83, v83
	s_waitcnt lgkmcnt(6)
	v_mfma_f32_32x32x16_bf16 v[64:79], v[176:179], v[104:107], v[64:79]
	s_add_u32 s8, s15, 0x23a60000
	v_exp_f32_e32 v84, v84
	v_exp_f32_e32 v85, v85
	v_exp_f32_e32 v86, v86
	v_exp_f32_e32 v87, v87
	v_mfma_f32_32x32x16_bf16 v[64:79], v[172:175], v[108:111], v[64:79]
	s_addc_u32 s9, s14, 0
	v_add_f32_e32 v172, v194, v80
	v_add_f32_e32 v173, v195, v81
	v_add_f32_e32 v172, v82, v172
	v_add_f32_e32 v173, v83, v173
	v_add_f32_e32 v172, v84, v172
	v_add_f32_e32 v173, v85, v173
	v_add_f32_e32 v194, v86, v172
	v_add_f32_e32 v195, v87, v173
	v_cvt_pk_bf16_f32 v172, v80, v81
	v_cvt_pk_bf16_f32 v173, v82, v83
	v_cvt_pk_bf16_f32 v174, v84, v85
	v_cvt_pk_bf16_f32 v175, v86, v87
	s_waitcnt lgkmcnt(2)
	v_mfma_f32_32x32x16_bf16 v[64:79], v[168:171], v[112:115], v[64:79]
	ds_read_b128 v[168:171], v209 offset:0x4000
	ds_read_b128 v[176:179], v210 offset:0x4000
	v_mfma_f32_32x32x16_bf16 v[64:79], v[164:167], v[116:119], v[64:79]
	v_exp_f32_e32 v88, v88
	v_exp_f32_e32 v89, v89
	v_exp_f32_e32 v90, v90
	v_exp_f32_e32 v91, v91
	ds_read_b128 v[164:167], v209 offset:0x5000
	ds_read_b128 v[180:183], v210 offset:0x5000
	s_waitcnt lgkmcnt(4)
	v_mfma_f32_32x32x16_bf16 v[64:79], v[160:163], v[120:123], v[64:79]
	v_exp_f32_e32 v92, v92
	v_exp_f32_e32 v93, v93
	v_exp_f32_e32 v94, v94
	v_exp_f32_e32 v95, v95
	v_add_f32_e32 v160, v194, v88
	v_add_f32_e32 v161, v195, v89
	v_add_f32_e32 v160, v90, v160
	v_add_f32_e32 v161, v91, v161
	v_add_f32_e32 v160, v92, v160
	v_add_f32_e32 v161, v93, v161
	v_add_f32_e32 v194, v94, v160
	v_add_f32_e32 v195, v95, v161
	v_cvt_pk_bf16_f32 v160, v88, v89
	v_cvt_pk_bf16_f32 v161, v90, v91
	v_cvt_pk_bf16_f32 v162, v92, v93
	v_cvt_pk_bf16_f32 v163, v94, v95
	v_mfma_f32_32x32x16_bf16 v[64:79], v[230:233], v[124:127], v[64:79]
	s_waitcnt lgkmcnt(2)
	v_mfma_f32_32x32x16_bf16 v[48:63], v[168:171], v[172:175], v[48:63]
	v_mfma_f32_32x32x16_bf16 v[48:63], v[176:179], v[160:163], v[48:63]
	ds_read_b128 v[80:83], v209 offset:0x6000
	ds_read_b128 v[84:87], v210 offset:0x6000
	s_waitcnt lgkmcnt(2)
	v_mfma_f32_32x32x16_bf16 v[32:47], v[164:167], v[172:175], v[32:47]
	v_mfma_f32_32x32x16_bf16 v[32:47], v[180:183], v[160:163], v[32:47]
	ds_read_b128 v[88:91], v209 offset:0x7000
	ds_read_b128 v[92:95], v210 offset:0x7000
	s_nop 1
	v_exp_f32_e32 v64, v64
	v_exp_f32_e32 v65, v65
	v_exp_f32_e32 v66, v66
	v_exp_f32_e32 v67, v67
	v_exp_f32_e32 v68, v68
	v_exp_f32_e32 v69, v69
	v_exp_f32_e32 v70, v70
	v_exp_f32_e32 v71, v71
	v_add_f32_e32 v164, v194, v64
	v_add_f32_e32 v165, v195, v65
	v_add_f32_e32 v164, v66, v164
	v_add_f32_e32 v165, v67, v165
	v_add_f32_e32 v164, v68, v164
	v_add_f32_e32 v165, v69, v165
	v_add_f32_e32 v168, v70, v164
	v_add_f32_e32 v169, v71, v165
	v_cvt_pk_bf16_f32 v164, v64, v65
	v_cvt_pk_bf16_f32 v165, v66, v67
	v_cvt_pk_bf16_f32 v166, v68, v69
	v_cvt_pk_bf16_f32 v167, v70, v71
	s_waitcnt lgkmcnt(2)
	v_mfma_f32_32x32x16_bf16 v[16:31], v[80:83], v[172:175], v[16:31]
	v_mfma_f32_32x32x16_bf16 v[16:31], v[84:87], v[160:163], v[16:31]
	ds_read_b128 v[80:83], v211 offset:0x4000
	ds_read_b128 v[84:87], v224 offset:0x4000
	s_waitcnt lgkmcnt(2)
	v_mfma_f32_32x32x16_bf16 v[0:15], v[88:91], v[172:175], v[0:15]
	v_mfma_f32_32x32x16_bf16 v[0:15], v[92:95], v[160:163], v[0:15]
	ds_read_b128 v[88:91], v211 offset:0x5000
	ds_read_b128 v[92:95], v224 offset:0x5000
	v_exp_f32_e32 v72, v72
	v_exp_f32_e32 v73, v73
	v_exp_f32_e32 v74, v74
	v_exp_f32_e32 v75, v75
	v_exp_f32_e32 v76, v76
	v_exp_f32_e32 v77, v77
	v_exp_f32_e32 v78, v78
	v_exp_f32_e32 v79, v79
	v_add_f32_e32 v160, v168, v72
	v_add_f32_e32 v161, v169, v73
	v_add_f32_e32 v160, v74, v160
	v_add_f32_e32 v161, v75, v161
	v_add_f32_e32 v160, v76, v160
	v_add_f32_e32 v161, v77, v161
	v_add_f32_e32 v194, v78, v160
	v_add_f32_e32 v195, v79, v161
	v_cvt_pk_bf16_f32 v160, v72, v73
	v_cvt_pk_bf16_f32 v161, v74, v75
	v_cvt_pk_bf16_f32 v162, v76, v77
	v_cvt_pk_bf16_f32 v163, v78, v79
	s_waitcnt lgkmcnt(2)
	v_mfma_f32_32x32x16_bf16 v[48:63], v[80:83], v[164:167], v[48:63]
	v_mfma_f32_32x32x16_bf16 v[48:63], v[84:87], v[160:163], v[48:63]
	ds_read_b128 v[64:67], v211 offset:0x6000
	ds_read_b128 v[68:71], v224 offset:0x6000
	s_waitcnt lgkmcnt(2)
	v_mfma_f32_32x32x16_bf16 v[32:47], v[88:91], v[164:167], v[32:47]
	v_mfma_f32_32x32x16_bf16 v[32:47], v[92:95], v[160:163], v[32:47]
	ds_read_b128 v[72:75], v211 offset:0x7000
	ds_read_b128 v[76:79], v224 offset:0x7000
	s_waitcnt lgkmcnt(2)
	v_mfma_f32_32x32x16_bf16 v[16:31], v[64:67], v[164:167], v[16:31]
	v_mfma_f32_32x32x16_bf16 v[16:31], v[68:71], v[160:163], v[16:31]
	s_waitcnt lgkmcnt(0)
	v_mfma_f32_32x32x16_bf16 v[0:15], v[72:75], v[164:167], v[0:15]
	v_mfma_f32_32x32x16_bf16 v[0:15], v[76:79], v[160:163], v[0:15]
	s_waitcnt lgkmcnt(0)
	s_barrier
	ds_read_b128 v[64:67], v201 offset:0x8000
	ds_read_b128 v[68:71], v202 offset:0x8000
	ds_read_b128 v[72:75], v203 offset:0x8000
	ds_read_b128 v[76:79], v204 offset:0x8000
	ds_read_b128 v[160:163], v205 offset:0x8000
	ds_read_b128 v[164:167], v206 offset:0x8000
	s_waitcnt lgkmcnt(4)
	v_mfma_f32_32x32x16_bf16 v[80:95], v[64:67], v[96:99], 0
	ds_read_b128 v[230:233], v207 offset:0x8000
	v_mfma_f32_32x32x16_bf16 v[80:95], v[68:71], v[100:103], v[80:95]
	ds_read_b128 v[64:67], v208 offset:0x8000
	s_waitcnt vmcnt(4)
	ds_write_b128 v225, v[140:143] offset:0
	s_waitcnt lgkmcnt(5)
	v_mfma_f32_32x32x16_bf16 v[80:95], v[72:75], v[104:107], v[80:95]
	ds_read_b128 v[140:143], v201 offset:0xa000
	ds_write_b128 v226, v[136:139] offset:0
	v_mfma_f32_32x32x16_bf16 v[80:95], v[76:79], v[108:111], v[80:95]
	ds_read_b128 v[180:183], v202 offset:0xa000
	ds_write_b64 v227, v[132:133] offset:0
	s_waitcnt lgkmcnt(7)
	v_mfma_f32_32x32x16_bf16 v[80:95], v[160:163], v[112:115], v[80:95]
	ds_read_b128 v[176:179], v203 offset:0xa000
	ds_write_b64 v228, v[134:135] offset:0
	v_mfma_f32_32x32x16_bf16 v[80:95], v[164:167], v[116:119], v[80:95]
	ds_read_b128 v[172:175], v204 offset:0xa000
	ds_write_b64 v229, v[128:129] offset:0
	s_waitcnt lgkmcnt(9)
	v_mfma_f32_32x32x16_bf16 v[80:95], v[230:233], v[120:123], v[80:95]
	ds_read_b128 v[168:171], v205 offset:0xa000
	ds_write_b64 v184, v[130:131] offset:0
	v_mfma_f32_32x32x16_bf16 v[80:95], v[64:67], v[124:127], v[80:95]
	ds_read_b128 v[164:167], v206 offset:0xa000
	s_waitcnt lgkmcnt(8)
	v_mfma_f32_32x32x16_bf16 v[64:79], v[140:143], v[96:99], 0
	ds_read_b128 v[160:163], v207 offset:0xa000
	global_load_dwordx4 v[132:135], v198, s[6:7]
	global_load_dwordx4 v[128:131], v199, s[6:7]
	global_load_dwordx4 v[136:139], v196, s[8:9]
	global_load_dwordx4 v[140:143], v197, s[8:9]
	s_add_u32 s6, s16, 0x3bc00380
	v_mfma_f32_32x32x16_bf16 v[64:79], v[180:183], v[100:103], v[64:79]
	ds_read_b128 v[230:233], v208 offset:0xa000
	s_addc_u32 s7, s17, 0
	v_exp_f32_e32 v80, v80
	v_exp_f32_e32 v81, v81
	v_exp_f32_e32 v82, v82
	v_exp_f32_e32 v83, v83
	s_waitcnt lgkmcnt(6)
	v_mfma_f32_32x32x16_bf16 v[64:79], v[176:179], v[104:107], v[64:79]
	s_add_u32 s8, s15, 0x23a70000
	v_exp_f32_e32 v84, v84
	v_exp_f32_e32 v85, v85
	v_exp_f32_e32 v86, v86
	v_exp_f32_e32 v87, v87
	v_mfma_f32_32x32x16_bf16 v[64:79], v[172:175], v[108:111], v[64:79]
	s_addc_u32 s9, s14, 0
	v_add_f32_e32 v172, v194, v80
	v_add_f32_e32 v173, v195, v81
	v_add_f32_e32 v172, v82, v172
	v_add_f32_e32 v173, v83, v173
	v_add_f32_e32 v172, v84, v172
	v_add_f32_e32 v173, v85, v173
	v_add_f32_e32 v194, v86, v172
	v_add_f32_e32 v195, v87, v173
	v_cvt_pk_bf16_f32 v172, v80, v81
	v_cvt_pk_bf16_f32 v173, v82, v83
	v_cvt_pk_bf16_f32 v174, v84, v85
	v_cvt_pk_bf16_f32 v175, v86, v87
	s_waitcnt lgkmcnt(2)
	v_mfma_f32_32x32x16_bf16 v[64:79], v[168:171], v[112:115], v[64:79]
	ds_read_b128 v[168:171], v209 offset:0x8000
	ds_read_b128 v[176:179], v210 offset:0x8000
	v_mfma_f32_32x32x16_bf16 v[64:79], v[164:167], v[116:119], v[64:79]
	v_exp_f32_e32 v88, v88
	v_exp_f32_e32 v89, v89
	v_exp_f32_e32 v90, v90
	v_exp_f32_e32 v91, v91
	ds_read_b128 v[164:167], v209 offset:0x9000
	ds_read_b128 v[180:183], v210 offset:0x9000
	s_waitcnt lgkmcnt(4)
	v_mfma_f32_32x32x16_bf16 v[64:79], v[160:163], v[120:123], v[64:79]
	v_exp_f32_e32 v92, v92
	v_exp_f32_e32 v93, v93
	v_exp_f32_e32 v94, v94
	v_exp_f32_e32 v95, v95
	v_add_f32_e32 v160, v194, v88
	v_add_f32_e32 v161, v195, v89
	v_add_f32_e32 v160, v90, v160
	v_add_f32_e32 v161, v91, v161
	v_add_f32_e32 v160, v92, v160
	v_add_f32_e32 v161, v93, v161
	v_add_f32_e32 v194, v94, v160
	v_add_f32_e32 v195, v95, v161
	v_cvt_pk_bf16_f32 v160, v88, v89
	v_cvt_pk_bf16_f32 v161, v90, v91
	v_cvt_pk_bf16_f32 v162, v92, v93
	v_cvt_pk_bf16_f32 v163, v94, v95
	v_mfma_f32_32x32x16_bf16 v[64:79], v[230:233], v[124:127], v[64:79]
	s_waitcnt lgkmcnt(2)
	v_mfma_f32_32x32x16_bf16 v[48:63], v[168:171], v[172:175], v[48:63]
	v_mfma_f32_32x32x16_bf16 v[48:63], v[176:179], v[160:163], v[48:63]
	ds_read_b128 v[80:83], v209 offset:0xa000
	ds_read_b128 v[84:87], v210 offset:0xa000
	s_waitcnt lgkmcnt(2)
	v_mfma_f32_32x32x16_bf16 v[32:47], v[164:167], v[172:175], v[32:47]
	v_mfma_f32_32x32x16_bf16 v[32:47], v[180:183], v[160:163], v[32:47]
	ds_read_b128 v[88:91], v209 offset:0xb000
	ds_read_b128 v[92:95], v210 offset:0xb000
	s_nop 1
	v_exp_f32_e32 v64, v64
	v_exp_f32_e32 v65, v65
	v_exp_f32_e32 v66, v66
	v_exp_f32_e32 v67, v67
	v_exp_f32_e32 v68, v68
	v_exp_f32_e32 v69, v69
	v_exp_f32_e32 v70, v70
	v_exp_f32_e32 v71, v71
	v_add_f32_e32 v164, v194, v64
	v_add_f32_e32 v165, v195, v65
	v_add_f32_e32 v164, v66, v164
	v_add_f32_e32 v165, v67, v165
	v_add_f32_e32 v164, v68, v164
	v_add_f32_e32 v165, v69, v165
	v_add_f32_e32 v168, v70, v164
	v_add_f32_e32 v169, v71, v165
	v_cvt_pk_bf16_f32 v164, v64, v65
	v_cvt_pk_bf16_f32 v165, v66, v67
	v_cvt_pk_bf16_f32 v166, v68, v69
	v_cvt_pk_bf16_f32 v167, v70, v71
	s_waitcnt lgkmcnt(2)
	v_mfma_f32_32x32x16_bf16 v[16:31], v[80:83], v[172:175], v[16:31]
	v_mfma_f32_32x32x16_bf16 v[16:31], v[84:87], v[160:163], v[16:31]
	ds_read_b128 v[80:83], v211 offset:0x8000
	ds_read_b128 v[84:87], v224 offset:0x8000
	s_waitcnt lgkmcnt(2)
	v_mfma_f32_32x32x16_bf16 v[0:15], v[88:91], v[172:175], v[0:15]
	v_mfma_f32_32x32x16_bf16 v[0:15], v[92:95], v[160:163], v[0:15]
	ds_read_b128 v[88:91], v211 offset:0x9000
	ds_read_b128 v[92:95], v224 offset:0x9000
	v_exp_f32_e32 v72, v72
	v_exp_f32_e32 v73, v73
	v_exp_f32_e32 v74, v74
	v_exp_f32_e32 v75, v75
	v_exp_f32_e32 v76, v76
	v_exp_f32_e32 v77, v77
	v_exp_f32_e32 v78, v78
	v_exp_f32_e32 v79, v79
	v_add_f32_e32 v160, v168, v72
	v_add_f32_e32 v161, v169, v73
	v_add_f32_e32 v160, v74, v160
	v_add_f32_e32 v161, v75, v161
	v_add_f32_e32 v160, v76, v160
	v_add_f32_e32 v161, v77, v161
	v_add_f32_e32 v194, v78, v160
	v_add_f32_e32 v195, v79, v161
	v_cvt_pk_bf16_f32 v160, v72, v73
	v_cvt_pk_bf16_f32 v161, v74, v75
	v_cvt_pk_bf16_f32 v162, v76, v77
	v_cvt_pk_bf16_f32 v163, v78, v79
	s_waitcnt lgkmcnt(2)
	v_mfma_f32_32x32x16_bf16 v[48:63], v[80:83], v[164:167], v[48:63]
	v_mfma_f32_32x32x16_bf16 v[48:63], v[84:87], v[160:163], v[48:63]
	ds_read_b128 v[64:67], v211 offset:0xa000
	ds_read_b128 v[68:71], v224 offset:0xa000
	s_waitcnt lgkmcnt(2)
	v_mfma_f32_32x32x16_bf16 v[32:47], v[88:91], v[164:167], v[32:47]
	v_mfma_f32_32x32x16_bf16 v[32:47], v[92:95], v[160:163], v[32:47]
	ds_read_b128 v[72:75], v211 offset:0xb000
	ds_read_b128 v[76:79], v224 offset:0xb000
	s_waitcnt lgkmcnt(2)
	v_mfma_f32_32x32x16_bf16 v[16:31], v[64:67], v[164:167], v[16:31]
	v_mfma_f32_32x32x16_bf16 v[16:31], v[68:71], v[160:163], v[16:31]
	s_waitcnt lgkmcnt(0)
	v_mfma_f32_32x32x16_bf16 v[0:15], v[72:75], v[164:167], v[0:15]
	v_mfma_f32_32x32x16_bf16 v[0:15], v[76:79], v[160:163], v[0:15]
	ds_read_b128 v[64:67], v201 offset:0xc000
	ds_read_b128 v[68:71], v202 offset:0xc000
	ds_read_b128 v[72:75], v203 offset:0xc000
	ds_read_b128 v[76:79], v204 offset:0xc000
	ds_read_b128 v[160:163], v205 offset:0xc000
	ds_read_b128 v[164:167], v206 offset:0xc000
	s_waitcnt lgkmcnt(4)
	v_mfma_f32_32x32x16_bf16 v[80:95], v[64:67], v[96:99], 0
	ds_read_b128 v[168:171], v207 offset:0xc000
	v_mfma_f32_32x32x16_bf16 v[80:95], v[68:71], v[100:103], v[80:95]
	ds_read_b128 v[64:67], v208 offset:0xc000
	s_waitcnt vmcnt(4)
	ds_write_b128 v225, v[156:159] offset:0x4000
	s_waitcnt lgkmcnt(5)
	v_mfma_f32_32x32x16_bf16 v[80:95], v[72:75], v[104:107], v[80:95]
	ds_read_b128 v[156:159], v201 offset:0xe000
	ds_write_b128 v226, v[152:155] offset:0x4000
	v_mfma_f32_32x32x16_bf16 v[80:95], v[76:79], v[108:111], v[80:95]
	ds_read_b128 v[172:175], v202 offset:0xe000
	ds_write_b64 v227, v[148:149] offset:0x4000
	s_waitcnt lgkmcnt(7)
	v_mfma_f32_32x32x16_bf16 v[80:95], v[160:163], v[112:115], v[80:95]
	ds_read_b128 v[176:179], v203 offset:0xe000
	ds_write_b64 v228, v[150:151] offset:0x4000
	v_mfma_f32_32x32x16_bf16 v[80:95], v[164:167], v[116:119], v[80:95]
	ds_read_b128 v[160:163], v204 offset:0xe000
	ds_write_b64 v229, v[144:145] offset:0x4000
	s_waitcnt lgkmcnt(9)
	v_mfma_f32_32x32x16_bf16 v[80:95], v[168:171], v[120:123], v[80:95]
	ds_read_b128 v[164:167], v205 offset:0xe000
	ds_write_b64 v184, v[146:147] offset:0x4000
	v_mfma_f32_32x32x16_bf16 v[80:95], v[64:67], v[124:127], v[80:95]
	ds_read_b128 v[168:171], v206 offset:0xe000
	s_waitcnt lgkmcnt(8)
	v_mfma_f32_32x32x16_bf16 v[64:79], v[156:159], v[96:99], 0
	ds_read_b128 v[180:183], v207 offset:0xe000
	global_load_dwordx4 v[148:151], v198, s[6:7]
	global_load_dwordx4 v[144:147], v199, s[6:7]
	global_load_dwordx4 v[152:155], v196, s[8:9]
	global_load_dwordx4 v[156:159], v197, s[8:9]
	s_add_i32 s8, s4, 4
	v_mfma_f32_32x32x16_bf16 v[64:79], v[172:175], v[100:103], v[64:79]
	ds_read_b128 v[230:233], v208 offset:0xe000
	s_cmpk_lt_u32 s4, 0x100
	v_exp_f32_e32 v80, v80
	v_exp_f32_e32 v81, v81
	v_exp_f32_e32 v82, v82
	v_exp_f32_e32 v83, v83
	s_waitcnt lgkmcnt(6)
	v_mfma_f32_32x32x16_bf16 v[64:79], v[176:179], v[104:107], v[64:79]
	s_cselect_b64 s[6:7], -1, 0
	v_exp_f32_e32 v84, v84
	v_exp_f32_e32 v85, v85
	v_exp_f32_e32 v86, v86
	v_exp_f32_e32 v87, v87
	v_mfma_f32_32x32x16_bf16 v[64:79], v[160:163], v[108:111], v[64:79]
	s_and_b64 s[6:7], s[0:1], s[6:7]
	v_add_f32_e32 v160, v194, v80
	v_add_f32_e32 v161, v195, v81
	s_add_u32 s10, s10, 0x200
	v_add_f32_e32 v160, v82, v160
	v_add_f32_e32 v161, v83, v161
	s_addc_u32 s11, s11, 0
	v_add_f32_e32 v160, v84, v160
	v_add_f32_e32 v161, v85, v161
	s_add_u32 s12, s12, 0x40000
	v_add_f32_e32 v194, v86, v160
	v_add_f32_e32 v195, v87, v161
	v_cvt_pk_bf16_f32 v160, v80, v81
	v_cvt_pk_bf16_f32 v161, v82, v83
	v_cvt_pk_bf16_f32 v162, v84, v85
	v_cvt_pk_bf16_f32 v163, v86, v87
	s_waitcnt lgkmcnt(2)
	v_mfma_f32_32x32x16_bf16 v[64:79], v[164:167], v[112:115], v[64:79]
	s_addc_u32 s13, s13, 0
	ds_read_b128 v[164:167], v209 offset:0xc000
	ds_read_b128 v[172:175], v210 offset:0xc000
	v_mfma_f32_32x32x16_bf16 v[64:79], v[168:171], v[116:119], v[64:79]
	s_and_b64 vcc, exec, s[6:7]
	v_exp_f32_e32 v88, v88
	v_exp_f32_e32 v89, v89
	v_exp_f32_e32 v90, v90
	v_exp_f32_e32 v91, v91
	ds_read_b128 v[168:171], v209 offset:0xd000
	ds_read_b128 v[176:179], v210 offset:0xd000
	s_waitcnt lgkmcnt(4)
	v_mfma_f32_32x32x16_bf16 v[64:79], v[180:183], v[120:123], v[64:79]
	s_mov_b32 s4, s8
	v_exp_f32_e32 v92, v92
	v_exp_f32_e32 v93, v93
	v_exp_f32_e32 v94, v94
	v_exp_f32_e32 v95, v95
	v_add_f32_e32 v180, v194, v88
	v_add_f32_e32 v181, v195, v89
	v_add_f32_e32 v180, v90, v180
	v_add_f32_e32 v181, v91, v181
	v_add_f32_e32 v180, v92, v180
	v_add_f32_e32 v181, v93, v181
	v_add_f32_e32 v194, v94, v180
	v_add_f32_e32 v195, v95, v181
	v_cvt_pk_bf16_f32 v180, v88, v89
	v_cvt_pk_bf16_f32 v181, v90, v91
	v_cvt_pk_bf16_f32 v182, v92, v93
	v_cvt_pk_bf16_f32 v183, v94, v95
	v_mfma_f32_32x32x16_bf16 v[64:79], v[230:233], v[124:127], v[64:79]
	s_waitcnt lgkmcnt(2)
	v_mfma_f32_32x32x16_bf16 v[48:63], v[164:167], v[160:163], v[48:63]
	v_mfma_f32_32x32x16_bf16 v[48:63], v[172:175], v[180:183], v[48:63]
	ds_read_b128 v[80:83], v209 offset:0xe000
	ds_read_b128 v[84:87], v210 offset:0xe000
	s_waitcnt lgkmcnt(2)
	v_mfma_f32_32x32x16_bf16 v[32:47], v[168:171], v[160:163], v[32:47]
	v_mfma_f32_32x32x16_bf16 v[32:47], v[176:179], v[180:183], v[32:47]
	ds_read_b128 v[88:91], v209 offset:0xf000
	ds_read_b128 v[92:95], v210 offset:0xf000
	s_nop 1
	v_exp_f32_e32 v64, v64
	v_exp_f32_e32 v65, v65
	v_exp_f32_e32 v66, v66
	v_exp_f32_e32 v67, v67
	v_exp_f32_e32 v68, v68
	v_exp_f32_e32 v69, v69
	v_exp_f32_e32 v70, v70
	v_exp_f32_e32 v71, v71
	v_add_f32_e32 v164, v194, v64
	v_add_f32_e32 v165, v195, v65
	v_add_f32_e32 v164, v66, v164
	v_add_f32_e32 v165, v67, v165
	v_add_f32_e32 v164, v68, v164
	v_add_f32_e32 v165, v69, v165
	v_add_f32_e32 v168, v70, v164
	v_add_f32_e32 v169, v71, v165
	v_cvt_pk_bf16_f32 v164, v64, v65
	v_cvt_pk_bf16_f32 v165, v66, v67
	v_cvt_pk_bf16_f32 v166, v68, v69
	v_cvt_pk_bf16_f32 v167, v70, v71
	s_waitcnt lgkmcnt(2)
	v_mfma_f32_32x32x16_bf16 v[16:31], v[80:83], v[160:163], v[16:31]
	v_mfma_f32_32x32x16_bf16 v[16:31], v[84:87], v[180:183], v[16:31]
	ds_read_b128 v[80:83], v211 offset:0xc000
	ds_read_b128 v[84:87], v224 offset:0xc000
	s_waitcnt lgkmcnt(2)
	v_mfma_f32_32x32x16_bf16 v[0:15], v[88:91], v[160:163], v[0:15]
	v_mfma_f32_32x32x16_bf16 v[0:15], v[92:95], v[180:183], v[0:15]
	ds_read_b128 v[88:91], v211 offset:0xd000
	ds_read_b128 v[92:95], v224 offset:0xd000
	v_exp_f32_e32 v72, v72
	v_exp_f32_e32 v73, v73
	v_exp_f32_e32 v74, v74
	v_exp_f32_e32 v75, v75
	v_exp_f32_e32 v76, v76
	v_exp_f32_e32 v77, v77
	v_exp_f32_e32 v78, v78
	v_exp_f32_e32 v79, v79
	v_add_f32_e32 v160, v168, v72
	v_add_f32_e32 v161, v169, v73
	v_cvt_pk_bf16_f32 v168, v72, v73
	v_cvt_pk_bf16_f32 v169, v74, v75
	v_cvt_pk_bf16_f32 v170, v76, v77
	v_cvt_pk_bf16_f32 v171, v78, v79
	v_add_f32_e32 v160, v74, v160
	v_add_f32_e32 v161, v75, v161
	v_add_f32_e32 v160, v76, v160
	v_add_f32_e32 v161, v77, v161
	v_add_f32_e32 v160, v78, v160
	v_add_f32_e32 v161, v79, v161
	s_waitcnt lgkmcnt(2)
	v_mfma_f32_32x32x16_bf16 v[48:63], v[80:83], v[164:167], v[48:63]
	v_mfma_f32_32x32x16_bf16 v[48:63], v[84:87], v[168:171], v[48:63]
	ds_read_b128 v[64:67], v211 offset:0xe000
	ds_read_b128 v[68:71], v224 offset:0xe000
	s_waitcnt lgkmcnt(2)
	v_mfma_f32_32x32x16_bf16 v[32:47], v[88:91], v[164:167], v[32:47]
	v_mfma_f32_32x32x16_bf16 v[32:47], v[92:95], v[168:171], v[32:47]
	ds_read_b128 v[72:75], v211 offset:0xf000
	ds_read_b128 v[76:79], v224 offset:0xf000
	s_waitcnt lgkmcnt(2)
	v_mfma_f32_32x32x16_bf16 v[16:31], v[64:67], v[164:167], v[16:31]
	v_mfma_f32_32x32x16_bf16 v[16:31], v[68:71], v[168:171], v[16:31]
	s_waitcnt lgkmcnt(0)
	v_mfma_f32_32x32x16_bf16 v[0:15], v[72:75], v[164:167], v[0:15]
	v_mfma_f32_32x32x16_bf16 v[0:15], v[76:79], v[168:171], v[0:15]
	s_cbranch_vccnz .LBB0_734
	v_pk_add_f32 v[64:65], v[160:161], v[160:161] op_sel:[0,1] op_sel_hi:[1,0]
	s_waitcnt vmcnt(0)
	s_nop 15
	s_nop 15
	v_mbcnt_lo_u32_b32 v67, -1, 0
	v_mbcnt_hi_u32_b32 v67, -1, v67
	s_nop 0
	v_mov_b32_e32 v65, v64
	s_nop 1
	v_permlane32_swap_b32_e32 v64, v65
	v_add_f32_e32 v64, v64, v65
	v_rcp_f32_e32 v66, v64
	v_and_or_b32 v64, v67, 31, v200
	v_ashrrev_i32_e32 v65, 31, v64
	v_lshlrev_b64 v[64:65], 12, v[64:65]
	v_mul_f32_e32 v48, v48, v66
	v_mul_f32_e32 v49, v49, v66
	v_cvt_pk_bf16_f32 v48, v48, v49
	v_mul_f32_e32 v49, v50, v66
	v_mul_f32_e32 v50, v51, v66
	v_cvt_pk_bf16_f32 v49, v49, v50
	v_mul_f32_e32 v50, v52, v66
	v_mul_f32_e32 v51, v53, v66
	v_lshrrev_b32_e32 v67, 1, v67
	v_cvt_pk_bf16_f32 v50, v50, v51
	v_mul_f32_e32 v51, v54, v66
	v_lshl_add_u64 v[64:65], s[58:59], 0, v[64:65]
	v_and_b32_e32 v184, 16, v67
	v_mul_f32_e32 v52, v55, v66
	v_cvt_pk_bf16_f32 v51, v51, v52
	v_lshl_add_u64 v[64:65], v[64:65], 0, v[184:185]
	v_permlane32_swap_b32_e32 v48, v50
	v_permlane32_swap_b32_e32 v49, v51
	global_store_dwordx4 v[64:65], v[48:51], off
	v_mul_f32_e32 v52, v63, v66
	v_mul_f32_e32 v32, v32, v66
	v_mul_f32_e32 v48, v56, v66
	v_mul_f32_e32 v49, v57, v66
	v_cvt_pk_bf16_f32 v48, v48, v49
	v_mul_f32_e32 v49, v58, v66
	v_mul_f32_e32 v50, v59, v66
	v_cvt_pk_bf16_f32 v49, v49, v50
	v_mul_f32_e32 v50, v60, v66
	v_mul_f32_e32 v51, v61, v66
	v_cvt_pk_bf16_f32 v50, v50, v51
	v_mul_f32_e32 v51, v62, v66
	v_cvt_pk_bf16_f32 v51, v51, v52
	v_permlane32_swap_b32_e32 v48, v50
	s_nop 0
	v_permlane32_swap_b32_e32 v49, v51
	v_mul_f32_e32 v33, v33, v66
	global_store_dwordx4 v[64:65], v[48:51], off offset:32
	v_cvt_pk_bf16_f32 v32, v32, v33
	v_mul_f32_e32 v33, v34, v66
	v_mul_f32_e32 v34, v35, v66
	v_cvt_pk_bf16_f32 v33, v33, v34
	v_mul_f32_e32 v34, v36, v66
	v_mul_f32_e32 v35, v37, v66
	v_cvt_pk_bf16_f32 v34, v34, v35
	v_mul_f32_e32 v35, v38, v66
	v_mul_f32_e32 v36, v39, v66
	v_cvt_pk_bf16_f32 v35, v35, v36
	v_permlane32_swap_b32_e32 v32, v34
	v_permlane32_swap_b32_e32 v33, v35
	global_store_dwordx4 v[64:65], v[32:35], off offset:64
	v_mul_f32_e32 v36, v47, v66
	v_mul_f32_e32 v16, v16, v66
	v_mul_f32_e32 v32, v40, v66
	v_mul_f32_e32 v33, v41, v66
	v_cvt_pk_bf16_f32 v32, v32, v33
	v_mul_f32_e32 v33, v42, v66
	v_mul_f32_e32 v34, v43, v66
	v_cvt_pk_bf16_f32 v33, v33, v34
	v_mul_f32_e32 v34, v44, v66
	v_mul_f32_e32 v35, v45, v66
	v_cvt_pk_bf16_f32 v34, v34, v35
	v_mul_f32_e32 v35, v46, v66
	v_cvt_pk_bf16_f32 v35, v35, v36
	v_permlane32_swap_b32_e32 v32, v34
	s_nop 0
	v_permlane32_swap_b32_e32 v33, v35
	v_mul_f32_e32 v17, v17, v66
	global_store_dwordx4 v[64:65], v[32:35], off offset:96
	v_cvt_pk_bf16_f32 v16, v16, v17
	v_mul_f32_e32 v17, v18, v66
	v_mul_f32_e32 v18, v19, v66
	v_cvt_pk_bf16_f32 v17, v17, v18
	v_mul_f32_e32 v18, v20, v66
	v_mul_f32_e32 v19, v21, v66
	v_cvt_pk_bf16_f32 v18, v18, v19
	v_mul_f32_e32 v19, v22, v66
	v_mul_f32_e32 v20, v23, v66
	v_cvt_pk_bf16_f32 v19, v19, v20
	v_permlane32_swap_b32_e32 v16, v18
	v_permlane32_swap_b32_e32 v17, v19
	global_store_dwordx4 v[64:65], v[16:19], off offset:128
	v_mul_f32_e32 v20, v31, v66
	v_mul_f32_e32 v0, v0, v66
	v_mul_f32_e32 v16, v24, v66
	v_mul_f32_e32 v17, v25, v66
	v_cvt_pk_bf16_f32 v16, v16, v17
	v_mul_f32_e32 v17, v26, v66
	v_mul_f32_e32 v18, v27, v66
	v_cvt_pk_bf16_f32 v17, v17, v18
	v_mul_f32_e32 v18, v28, v66
	v_mul_f32_e32 v19, v29, v66
	v_cvt_pk_bf16_f32 v18, v18, v19
	v_mul_f32_e32 v19, v30, v66
	v_cvt_pk_bf16_f32 v19, v19, v20
	v_permlane32_swap_b32_e32 v16, v18
	s_nop 0
	v_permlane32_swap_b32_e32 v17, v19
	v_mul_f32_e32 v1, v1, v66
	global_store_dwordx4 v[64:65], v[16:19], off offset:160
	v_cvt_pk_bf16_f32 v0, v0, v1
	v_mul_f32_e32 v1, v2, v66
	v_mul_f32_e32 v2, v3, v66
	v_cvt_pk_bf16_f32 v1, v1, v2
	v_mul_f32_e32 v2, v4, v66
	v_mul_f32_e32 v3, v5, v66
	v_cvt_pk_bf16_f32 v2, v2, v3
	v_mul_f32_e32 v3, v6, v66
	v_mul_f32_e32 v4, v7, v66
	v_cvt_pk_bf16_f32 v3, v3, v4
	v_permlane32_swap_b32_e32 v0, v2
	v_permlane32_swap_b32_e32 v1, v3
	global_store_dwordx4 v[64:65], v[0:3], off offset:192
	v_mul_f32_e32 v4, v15, v66
	s_nop 0
	v_mul_f32_e32 v0, v8, v66
	v_mul_f32_e32 v1, v9, v66
	v_cvt_pk_bf16_f32 v0, v0, v1
	v_mul_f32_e32 v1, v10, v66
	v_mul_f32_e32 v2, v11, v66
	v_cvt_pk_bf16_f32 v1, v1, v2
	v_mul_f32_e32 v2, v12, v66
	v_mul_f32_e32 v3, v13, v66
	v_cvt_pk_bf16_f32 v2, v2, v3
	v_mul_f32_e32 v3, v14, v66
	v_cvt_pk_bf16_f32 v3, v3, v4
	v_permlane32_swap_b32_e32 v0, v2
	s_nop 0
	v_permlane32_swap_b32_e32 v1, v3
	global_store_dwordx4 v[64:65], v[0:3], off offset:224
	s_barrier
